# speedup vs baseline: 1.0018x; 1.0018x over previous
.LBB1_50:
	s_waitcnt lgkmcnt(0)
	s_barrier
	s_cmpk_gt_u32 s36, 0xff
	s_cbranch_scc1 .LBB1_54
	s_setprio 2
	s_nop 0
	s_and_saveexec_b64 s[2:3], s[0:1]
	s_cbranch_execz .LBB1_53
	s_and_b32 s5, s36, 0xc0
	s_lshl_b32 s5, s5, 2
	s_add_i32 s5, s5, 0
	s_add_i32 s5, s5, 0x18000
	v_lshl_add_u32 v35, v202, 2, s5
	v_add_u32_e32 v35, 0x400, v35
	ds_read2_b32 v[36:37], v35 offset1:32
	v_max_f32_e32 v35, v192, v192
	s_waitcnt lgkmcnt(0)
	v_max_f32_e32 v38, v36, v36
	v_max_f32_e32 v35, v35, v38
	v_sub_f32_e32 v38, v192, v35
	v_sub_f32_e32 v35, v36, v35
	v_exp_f32_e32 v35, v35
	v_exp_f32_e32 v36, v38
	v_mul_f32_e32 v37, v37, v35
	v_fmac_f32_e32 v37, v34, v36
	v_rcp_f32_e32 v34, v37
	s_nop 0
	v_mul_f32_e32 v36, v36, v34
	v_mul_f32_e32 v34, v35, v34
	ds_write2_b32 v214, v36, v34 offset1:32

.LBB1_57:
	v_add_u32_e32 v0, s2, v191
	v_add3_u32 v197, v0, v209, v210
	v_max_f32_e32 v0, v33, v33
	v_max_f32_e32 v2, v32, v32
	v_max_f32_e32 v0, v2, v0
	v_max3_f32 v2, v34, v35, v17
	v_max3_f32 v0, v0, v16, v18
	v_max3_f32 v0, v0, v19, v36
	v_max3_f32 v2, v2, v38, v39
	v_max3_f32 v0, v0, v37, v20
	v_max3_f32 v2, v2, v22, v23
	v_max3_f32 v0, v0, v21, v40
	v_max3_f32 v2, v2, v42, v43
	v_max3_f32 v0, v0, v41, v24
	v_max3_f32 v2, v2, v26, v27
	v_max3_f32 v0, v0, v25, v44
	v_max3_f32 v2, v2, v46, v47
	v_max3_f32 v0, v0, v45, v28
	v_max3_f32 v2, v2, v30, v31
	v_max3_f32 v0, v0, v29, v2
	v_mov_b32_e32 v2, v0
	s_and_b32 s3, s23, 0x3fffffc0
	s_nop 0
	v_permlane32_swap_b32_e32 v0, v2
	s_lshl_b32 s2, s3, 2
	v_max_f32_e32 v2, v2, v2
	v_max_f32_e32 v0, v0, v0
	s_add_i32 s27, s2, 0
	v_max_f32_e32 v0, v0, v2
	s_mov_b32 s2, 0x41000000
	v_cmp_le_f32_e32 vcc, -4.0, v0
	v_cmp_ge_f32_e64 s[2:3], s2, v0
	v_max_f32_e32 v0, 0xf149f2ca, v0
	s_and_b64 s[2:3], vcc, s[2:3]
	v_cndmask_b32_e64 v192, v0, 0, s[2:3]
	v_add_f32_e64 v0, v32, -v192
	v_exp_f32_e32 v64, v0
	v_add_f32_e64 v0, v16, -v192
	v_exp_f32_e32 v32, v0
	v_add_f32_e64 v0, v33, -v192
	v_exp_f32_e32 v65, v0
	v_add_f32_e64 v0, v17, -v192
	v_exp_f32_e32 v33, v0
	v_add_f32_e64 v0, v34, -v192
	v_exp_f32_e32 v66, v0
	v_add_f32_e64 v0, v18, -v192
	v_exp_f32_e32 v34, v0
	v_add_f32_e64 v0, v35, -v192
	v_exp_f32_e32 v67, v0
	v_add_f32_e64 v0, v19, -v192
	v_exp_f32_e32 v35, v0
	v_add_f32_e64 v0, v36, -v192
	v_exp_f32_e32 v68, v0
	v_add_f32_e64 v0, v20, -v192
	v_exp_f32_e32 v36, v0
	v_add_f32_e64 v0, v37, -v192
	v_exp_f32_e32 v69, v0
	v_add_f32_e64 v0, v21, -v192
	v_exp_f32_e32 v37, v0
	v_add_f32_e64 v0, v38, -v192
	v_exp_f32_e32 v70, v0
	v_add_f32_e64 v0, v22, -v192
	v_exp_f32_e32 v38, v0
	v_add_f32_e64 v0, v39, -v192
	v_exp_f32_e32 v71, v0
	v_add_f32_e64 v0, v23, -v192
	v_exp_f32_e32 v39, v0
	v_add_f32_e64 v0, v40, -v192
	v_exp_f32_e32 v72, v0
	v_add_f32_e64 v0, v24, -v192
	v_exp_f32_e32 v40, v0
	v_add_f32_e64 v0, v41, -v192
	v_exp_f32_e32 v73, v0
	v_add_f32_e64 v0, v25, -v192
	v_exp_f32_e32 v41, v0
	v_add_f32_e64 v0, v42, -v192
	v_exp_f32_e32 v74, v0
	v_add_f32_e64 v0, v26, -v192
	v_exp_f32_e32 v42, v0
	v_add_f32_e64 v0, v43, -v192
	v_exp_f32_e32 v75, v0
	v_add_f32_e64 v0, v27, -v192
	v_exp_f32_e32 v43, v0
	v_add_f32_e64 v0, v44, -v192
	v_exp_f32_e32 v76, v0
	v_add_f32_e64 v0, v28, -v192
	v_exp_f32_e32 v44, v0
	v_add_f32_e64 v0, v45, -v192
	v_exp_f32_e32 v77, v0
	v_add_f32_e64 v0, v29, -v192
	v_exp_f32_e32 v45, v0
	v_add_f32_e64 v0, v46, -v192
	v_exp_f32_e32 v78, v0
	v_add_f32_e64 v0, v30, -v192
	v_exp_f32_e32 v46, v0
	v_add_f32_e64 v0, v47, -v192
	v_exp_f32_e32 v79, v0
	v_add_f32_e64 v0, v31, -v192
	v_exp_f32_e32 v47, v0
	s_bitcmp1_b32 s36, 8
	s_cbranch_scc1 .Lu2w_g1
	s_waitcnt vmcnt(4) lgkmcnt(0)
	s_setprio 0
	s_nop 0
	s_branch .Lu2w_done
